# P9/P10 epilogue heads: MFMA-write to VALU-read pad re-derived (s_nop 11 = 12 wait states for the 8-pass fp8 MFMA) instead of two s_nop 15
# speedup vs baseline: 1.0006x; 1.0006x over previous
; #define LAS __attribute__((address_space(3)))
; __device__ __forceinline__ unsigned pk4_fp8(float a, float b, float c, float d) { int w = 0; w = __builtin_amdgcn_cvt_pk_fp8_f32(a, b, w, false); w = __builtin_amdgcn_cvt_pk_fp8_f32(c, d, w, true); return (unsigned)w; }
;     __device__ __forceinline__ void operator()(const f32x4 (&acc)[2][2][4][2], const Unit& u, int wr, int wc, int fr, int fq) const {
;         const int e = u.pn / npn, pnl = u.pn - e * npn; const int tid = threadIdx.x;
;         const int col0 = pnl * BM + wc * 32 + 8 * fq;
;         f32x4 bv[2][2];
; #pragma unroll
;         for (int bj = 0; bj < 2; ++bj)
; #pragma unroll
;             for (int n = 0; n < 2; ++n) bv[bj][n] = *(const f32x4*)(bias + (size_t)e * bias_ld + col0 + bj * HALF + 4 * n);
;         LAS unsigned char* wp = stg + (16 * wr + fr) * STG8_PITCH + 16 * wc + 4 * fq;
;         const int rr = (tid >> 3) & 31, cc = tid & 7, ms = tid >> 8;
;         const LAS unsigned char* rp = stg + rr * STG8_PITCH + cc * 16;
;         unsigned char* gp = O + (size_t)(u.pm * BM + 64 * (rr >> 4) + (rr & 15)) * ldc + pnl * (BM / 2) + cc * 16;
; #pragma unroll
;         for (int ai = 0; ai < 2; ++ai) {
; #pragma unroll
;             for (int m = 0; m < 4; ++m)
; #pragma unroll
;                 for (int bj = 0; bj < 2; ++bj) { const f32x4 v0 = acc[ai][bj][m][0] * scale + bv[bj][0], v1 = acc[ai][bj][m][1] * scale + bv[bj][1];
;                     *(LAS unsigned*)(wp + m * (32 * STG8_PITCH) + 64 * bj) = pk4_fp8(swiglu1(v0[0], v0[1]), swiglu1(v0[2], v0[3]), swiglu1(v1[0], v1[1]), swiglu1(v1[2], v1[3])); }
.LBB0_1010:
	s_cmp_eq_u32 s42, s46
	s_cselect_b32 s55, s23, s19
	s_ashr_i32 s2, s23, 31
	s_lshr_b32 s2, s2, 28
	s_add_i32 s3, s23, s2
	s_and_b32 s3, s3, -16
	s_sub_i32 s23, s23, s3
	s_ashr_i32 s2, s55, 31
	s_lshr_b32 s2, s2, 28
	s_add_i32 s3, s55, s2
	s_ashr_i32 s2, s3, 4
	s_and_b32 s3, s3, -16
	s_sub_i32 s54, s55, s3
	s_ashr_i32 s3, s2, 31
	s_lshl_b64 s[2:3], s[2:3], 14
	v_readlane_b32 s52, v254, 0
	v_lshl_or_b32 v2, s54, 8, v200
	v_readlane_b32 s53, v254, 1
	s_add_u32 s2, s52, s2
	s_addc_u32 s3, s53, s3
	v_ashrrev_i32_e32 v3, 31, v2
	s_nop 11
	v_lshl_add_u64 v[2:3], v[2:3], 2, s[2:3]
	global_load_dwordx4 v[208:211], v[2:3], off
	global_load_dwordx4 v[212:215], v[2:3], off offset:16
	global_load_dwordx4 v[216:219], v[2:3], off offset:512
	global_load_dwordx4 v[220:223], v[2:3], off offset:528
	v_lshl_or_b32 v18, s22, 8, v201
	v_ashrrev_i32_e32 v19, 31, v18
	v_lshlrev_b64 v[18:19], 11, v[18:19]
	s_lshl_b32 s22, s23, 7
	v_lshl_add_u64 v[18:19], s[8:9], 0, v[18:19]
	s_ashr_i32 s23, s22, 31
	v_lshl_add_u64 v[18:19], v[18:19], 0, s[22:23]
	v_lshl_add_u64 v[18:19], v[18:19], 0, v[170:171]
	s_cmp_eq_u32 s42, s46
	s_mov_b64 s[2:3], -1
	v_readlane_b32 s54, v254, 2
	v_readlane_b32 s55, v254, 3
	v_readlane_b32 s56, v254, 4
	v_readlane_b32 s57, v254, 5
	v_readlane_b32 s58, v254, 6
	v_readlane_b32 s59, v254, 7
	v_add_u32_e32 v22, 0x1000, v202
	v_add_u32_e32 v23, 0x2400, v202
	v_add_u32_e32 v24, 0x3400, v202
	v_min_f32_e32 v158, 0x43e00000, v158
	v_min_f32_e32 v160, 0x43e00000, v160
	v_min_f32_e32 v154, 0x43e00000, v154
	v_min_f32_e32 v156, 0x43e00000, v156
	v_mul_f32_e32 v2, 0xbd1d265f, v158
	v_mul_f32_e32 v3, 0xbd1d265f, v160
	v_mul_f32_e32 v4, 0xbd1d265f, v154
	v_mul_f32_e32 v5, 0xbd1d265f, v156
	v_exp_f32_e32 v2, v2
	v_exp_f32_e32 v3, v3
	v_exp_f32_e32 v4, v4
	v_exp_f32_e32 v5, v5
	v_fma_f32 v2, v2, v246, v246
	v_fma_f32 v3, v3, v246, v246
	v_fma_f32 v4, v4, v246, v246
	v_fma_f32 v5, v5, v246, v246
	v_rcp_f32_e32 v2, v2
	v_rcp_f32_e32 v3, v3
	v_rcp_f32_e32 v4, v4
	v_rcp_f32_e32 v5, v5
	v_med3_f32 v159, v159, s47, v204
	v_med3_f32 v161, v161, s47, v204
	v_med3_f32 v155, v155, s47, v204
	v_med3_f32 v157, v157, s47, v204
	v_mul_f32_e32 v158, v158, v2
	v_mul_f32_e32 v160, v160, v3
	v_mul_f32_e32 v154, v154, v4
	v_mul_f32_e32 v156, v156, v5
	v_mul_f32_e32 v158, v158, v159
	v_mul_f32_e32 v160, v160, v161
	v_mul_f32_e32 v154, v154, v155
	v_mul_f32_e32 v156, v156, v157
	v_cvt_pk_fp8_f32 v6, v158, v160
	v_cvt_pk_fp8_f32 v6, v154, v156 op_sel:[0,0,1]
	v_min_f32_e32 v150, 0x43e00000, v150
	v_min_f32_e32 v152, 0x43e00000, v152
	v_min_f32_e32 v146, 0x43e00000, v146
	v_min_f32_e32 v148, 0x43e00000, v148
	v_mul_f32_e32 v2, 0xbd1d265f, v150
	v_mul_f32_e32 v3, 0xbd1d265f, v152
	v_mul_f32_e32 v4, 0xbd1d265f, v146
	v_mul_f32_e32 v5, 0xbd1d265f, v148
	v_exp_f32_e32 v2, v2
	v_exp_f32_e32 v3, v3
	v_exp_f32_e32 v4, v4
	v_exp_f32_e32 v5, v5
	v_fma_f32 v2, v2, v246, v246
	v_fma_f32 v3, v3, v246, v246
	v_fma_f32 v4, v4, v246, v246
	v_fma_f32 v5, v5, v246, v246
	v_rcp_f32_e32 v2, v2
	v_rcp_f32_e32 v3, v3
	v_rcp_f32_e32 v4, v4
	v_rcp_f32_e32 v5, v5
	v_med3_f32 v151, v151, s47, v204
	v_med3_f32 v153, v153, s47, v204
	v_med3_f32 v147, v147, s47, v204
	v_med3_f32 v149, v149, s47, v204
	v_mul_f32_e32 v150, v150, v2
	v_mul_f32_e32 v152, v152, v3
	v_mul_f32_e32 v146, v146, v4
	v_mul_f32_e32 v148, v148, v5
	v_mul_f32_e32 v150, v150, v151
	v_mul_f32_e32 v152, v152, v153
	v_mul_f32_e32 v146, v146, v147
	v_mul_f32_e32 v148, v148, v149
	v_cvt_pk_fp8_f32 v7, v150, v152
	v_cvt_pk_fp8_f32 v7, v146, v148 op_sel:[0,0,1]
	v_min_f32_e32 v142, 0x43e00000, v142
	v_min_f32_e32 v144, 0x43e00000, v144
	v_min_f32_e32 v138, 0x43e00000, v138
	v_min_f32_e32 v140, 0x43e00000, v140
	v_mul_f32_e32 v2, 0xbd1d265f, v142
	v_mul_f32_e32 v3, 0xbd1d265f, v144
	v_mul_f32_e32 v4, 0xbd1d265f, v138
	v_mul_f32_e32 v5, 0xbd1d265f, v140
	v_exp_f32_e32 v2, v2
	v_exp_f32_e32 v3, v3
	v_exp_f32_e32 v4, v4
	v_exp_f32_e32 v5, v5
	v_fma_f32 v2, v2, v246, v246
	v_fma_f32 v3, v3, v246, v246
	v_fma_f32 v4, v4, v246, v246
	v_fma_f32 v5, v5, v246, v246
	v_rcp_f32_e32 v2, v2
	v_rcp_f32_e32 v3, v3
	v_rcp_f32_e32 v4, v4
	v_rcp_f32_e32 v5, v5
	v_med3_f32 v143, v143, s47, v204
	v_med3_f32 v145, v145, s47, v204
	v_med3_f32 v139, v139, s47, v204
	v_med3_f32 v141, v141, s47, v204
	v_mul_f32_e32 v142, v142, v2
	v_mul_f32_e32 v144, v144, v3
	v_mul_f32_e32 v138, v138, v4
	v_mul_f32_e32 v140, v140, v5
	v_mul_f32_e32 v142, v142, v143
	v_mul_f32_e32 v144, v144, v145
	v_mul_f32_e32 v138, v138, v139
	v_mul_f32_e32 v140, v140, v141
	v_cvt_pk_fp8_f32 v8, v142, v144
	v_cvt_pk_fp8_f32 v8, v138, v140 op_sel:[0,0,1]
	v_min_f32_e32 v134, 0x43e00000, v134
	v_min_f32_e32 v136, 0x43e00000, v136
	v_min_f32_e32 v130, 0x43e00000, v130
	v_min_f32_e32 v132, 0x43e00000, v132
	v_mul_f32_e32 v2, 0xbd1d265f, v134
	v_mul_f32_e32 v3, 0xbd1d265f, v136
	v_mul_f32_e32 v4, 0xbd1d265f, v130
	v_mul_f32_e32 v5, 0xbd1d265f, v132
	v_exp_f32_e32 v2, v2
	v_exp_f32_e32 v3, v3
	v_exp_f32_e32 v4, v4
	v_exp_f32_e32 v5, v5
	v_fma_f32 v2, v2, v246, v246
	v_fma_f32 v3, v3, v246, v246
	v_fma_f32 v4, v4, v246, v246
	v_fma_f32 v5, v5, v246, v246
	v_rcp_f32_e32 v2, v2
	v_rcp_f32_e32 v3, v3
	v_rcp_f32_e32 v4, v4
	v_rcp_f32_e32 v5, v5
	v_med3_f32 v135, v135, s47, v204
	v_med3_f32 v137, v137, s47, v204
	v_med3_f32 v131, v131, s47, v204
	v_med3_f32 v133, v133, s47, v204
	v_mul_f32_e32 v134, v134, v2
	v_mul_f32_e32 v136, v136, v3
	v_mul_f32_e32 v130, v130, v4
	v_mul_f32_e32 v132, v132, v5
	v_mul_f32_e32 v134, v134, v135
	v_mul_f32_e32 v136, v136, v137
	v_mul_f32_e32 v130, v130, v131
	v_mul_f32_e32 v132, v132, v133
	v_cvt_pk_fp8_f32 v9, v134, v136
	v_cvt_pk_fp8_f32 v9, v130, v132 op_sel:[0,0,1]
; #define LAS __attribute__((address_space(3)))
; __device__ __forceinline__ unsigned pk4_fp8(float a, float b, float c, float d) { int w = 0; w = __builtin_amdgcn_cvt_pk_fp8_f32(a, b, w, false); w = __builtin_amdgcn_cvt_pk_fp8_f32(c, d, w, true); return (unsigned)w; }
;     __device__ __forceinline__ void operator()(const f32x4 (&acc)[2][2][4][2], const Unit& u, int wr, int wc, int fr, int fq) const {
;     ...
; #pragma unroll
;             for (int m = 0; m < 4; ++m)
; #pragma unroll
;                 for (int bj = 0; bj < 2; ++bj) { const f32x4 v0 = acc[ai][bj][m][0] * scale + bv[bj][0], v1 = acc[ai][bj][m][1] * scale + bv[bj][1];
;                     *(LAS unsigned*)(wp + m * (32 * STG8_PITCH) + 64 * bj) = pk4_fp8(swiglu1(v0[0], v0[1]), swiglu1(v0[2], v0[3]), swiglu1(v1[0], v1[1]), swiglu1(v1[2], v1[3])); }
	v_min_f32_e32 v126, 0x43e00000, v126
	v_min_f32_e32 v128, 0x43e00000, v128
	v_min_f32_e32 v122, 0x43e00000, v122
	v_min_f32_e32 v124, 0x43e00000, v124
	v_mul_f32_e32 v2, 0xbd1d265f, v126
	v_mul_f32_e32 v3, 0xbd1d265f, v128
	v_mul_f32_e32 v4, 0xbd1d265f, v122
	v_mul_f32_e32 v5, 0xbd1d265f, v124
	v_exp_f32_e32 v2, v2
	v_exp_f32_e32 v3, v3
	v_exp_f32_e32 v4, v4
	v_exp_f32_e32 v5, v5
	v_fma_f32 v2, v2, v246, v246
	v_fma_f32 v3, v3, v246, v246
	v_fma_f32 v4, v4, v246, v246
	v_fma_f32 v5, v5, v246, v246
	v_rcp_f32_e32 v2, v2
	v_rcp_f32_e32 v3, v3
	v_rcp_f32_e32 v4, v4
	v_rcp_f32_e32 v5, v5
	v_med3_f32 v127, v127, s47, v204
	v_med3_f32 v129, v129, s47, v204
	v_med3_f32 v123, v123, s47, v204
	v_med3_f32 v125, v125, s47, v204
	v_mul_f32_e32 v126, v126, v2
	v_mul_f32_e32 v128, v128, v3
	v_mul_f32_e32 v122, v122, v4
	v_mul_f32_e32 v124, v124, v5
	v_mul_f32_e32 v126, v126, v127
	v_mul_f32_e32 v128, v128, v129
	v_mul_f32_e32 v122, v122, v123
	v_mul_f32_e32 v124, v124, v125
	v_cvt_pk_fp8_f32 v10, v126, v128
	v_cvt_pk_fp8_f32 v10, v122, v124 op_sel:[0,0,1]
	v_min_f32_e32 v118, 0x43e00000, v118
	v_min_f32_e32 v120, 0x43e00000, v120
	v_min_f32_e32 v114, 0x43e00000, v114
	v_min_f32_e32 v116, 0x43e00000, v116
	v_mul_f32_e32 v2, 0xbd1d265f, v118
	v_mul_f32_e32 v3, 0xbd1d265f, v120
	v_mul_f32_e32 v4, 0xbd1d265f, v114
	v_mul_f32_e32 v5, 0xbd1d265f, v116
	v_exp_f32_e32 v2, v2
	v_exp_f32_e32 v3, v3
	v_exp_f32_e32 v4, v4
	v_exp_f32_e32 v5, v5
	v_fma_f32 v2, v2, v246, v246
	v_fma_f32 v3, v3, v246, v246
	v_fma_f32 v4, v4, v246, v246
	v_fma_f32 v5, v5, v246, v246
	v_rcp_f32_e32 v2, v2
	v_rcp_f32_e32 v3, v3
	v_rcp_f32_e32 v4, v4
	v_rcp_f32_e32 v5, v5
	v_med3_f32 v119, v119, s47, v204
	v_med3_f32 v121, v121, s47, v204
	v_med3_f32 v115, v115, s47, v204
	v_med3_f32 v117, v117, s47, v204
	v_mul_f32_e32 v118, v118, v2
	v_mul_f32_e32 v120, v120, v3
	v_mul_f32_e32 v114, v114, v4
	v_mul_f32_e32 v116, v116, v5
	v_mul_f32_e32 v118, v118, v119
	v_mul_f32_e32 v120, v120, v121
	v_mul_f32_e32 v114, v114, v115
	v_mul_f32_e32 v116, v116, v117
	v_cvt_pk_fp8_f32 v11, v118, v120
	v_cvt_pk_fp8_f32 v11, v114, v116 op_sel:[0,0,1]
	v_min_f32_e32 v110, 0x43e00000, v110
	v_min_f32_e32 v112, 0x43e00000, v112
	v_min_f32_e32 v106, 0x43e00000, v106
	v_min_f32_e32 v108, 0x43e00000, v108
	v_mul_f32_e32 v2, 0xbd1d265f, v110
	v_mul_f32_e32 v3, 0xbd1d265f, v112
	v_mul_f32_e32 v4, 0xbd1d265f, v106
	v_mul_f32_e32 v5, 0xbd1d265f, v108
	v_exp_f32_e32 v2, v2
	v_exp_f32_e32 v3, v3
	v_exp_f32_e32 v4, v4
	v_exp_f32_e32 v5, v5
	v_fma_f32 v2, v2, v246, v246
	v_fma_f32 v3, v3, v246, v246
	v_fma_f32 v4, v4, v246, v246
	v_fma_f32 v5, v5, v246, v246
	v_rcp_f32_e32 v2, v2
	v_rcp_f32_e32 v3, v3
	v_rcp_f32_e32 v4, v4
	v_rcp_f32_e32 v5, v5
	v_med3_f32 v111, v111, s47, v204
	v_med3_f32 v113, v113, s47, v204
	v_med3_f32 v107, v107, s47, v204
	v_med3_f32 v109, v109, s47, v204
	v_mul_f32_e32 v110, v110, v2
	v_mul_f32_e32 v112, v112, v3
	v_mul_f32_e32 v106, v106, v4
	v_mul_f32_e32 v108, v108, v5
	v_mul_f32_e32 v110, v110, v111
	v_mul_f32_e32 v112, v112, v113
	v_mul_f32_e32 v106, v106, v107
	v_mul_f32_e32 v108, v108, v109
	v_cvt_pk_fp8_f32 v12, v110, v112
	v_cvt_pk_fp8_f32 v12, v106, v108 op_sel:[0,0,1]
	v_min_f32_e32 v102, 0x43e00000, v102
	v_min_f32_e32 v104, 0x43e00000, v104
	v_min_f32_e32 v98, 0x43e00000, v98
	v_min_f32_e32 v100, 0x43e00000, v100
	v_mul_f32_e32 v2, 0xbd1d265f, v102
	v_mul_f32_e32 v3, 0xbd1d265f, v104
	v_mul_f32_e32 v4, 0xbd1d265f, v98
	v_mul_f32_e32 v5, 0xbd1d265f, v100
	v_exp_f32_e32 v2, v2
	v_exp_f32_e32 v3, v3
	v_exp_f32_e32 v4, v4
	v_exp_f32_e32 v5, v5
	v_fma_f32 v2, v2, v246, v246
	v_fma_f32 v3, v3, v246, v246
	v_fma_f32 v4, v4, v246, v246
	v_fma_f32 v5, v5, v246, v246
	v_rcp_f32_e32 v2, v2
	v_rcp_f32_e32 v3, v3
	v_rcp_f32_e32 v4, v4
	v_rcp_f32_e32 v5, v5
	v_med3_f32 v103, v103, s47, v204
	v_med3_f32 v105, v105, s47, v204
	v_med3_f32 v99, v99, s47, v204
	v_med3_f32 v101, v101, s47, v204
	v_mul_f32_e32 v102, v102, v2
	v_mul_f32_e32 v104, v104, v3
	v_mul_f32_e32 v98, v98, v4
	v_mul_f32_e32 v100, v100, v5
	v_mul_f32_e32 v102, v102, v103
	v_mul_f32_e32 v104, v104, v105
	v_mul_f32_e32 v98, v98, v99
	v_mul_f32_e32 v100, v100, v101
	v_cvt_pk_fp8_f32 v13, v102, v104
	v_cvt_pk_fp8_f32 v13, v98, v100 op_sel:[0,0,1]
	v_min_f32_e32 v94, 0x43e00000, v94
	v_min_f32_e32 v96, 0x43e00000, v96
	v_min_f32_e32 v90, 0x43e00000, v90
	v_min_f32_e32 v92, 0x43e00000, v92
	v_mul_f32_e32 v2, 0xbd1d265f, v94
	v_mul_f32_e32 v3, 0xbd1d265f, v96
	v_mul_f32_e32 v4, 0xbd1d265f, v90
	v_mul_f32_e32 v5, 0xbd1d265f, v92
	v_exp_f32_e32 v2, v2
	v_exp_f32_e32 v3, v3
	v_exp_f32_e32 v4, v4
	v_exp_f32_e32 v5, v5
	v_fma_f32 v2, v2, v246, v246
	v_fma_f32 v3, v3, v246, v246
	v_fma_f32 v4, v4, v246, v246
	v_fma_f32 v5, v5, v246, v246
	v_rcp_f32_e32 v2, v2
	v_rcp_f32_e32 v3, v3
	v_rcp_f32_e32 v4, v4
	v_rcp_f32_e32 v5, v5
	v_med3_f32 v95, v95, s47, v204
	v_med3_f32 v97, v97, s47, v204
	v_med3_f32 v91, v91, s47, v204
	v_med3_f32 v93, v93, s47, v204
	v_mul_f32_e32 v94, v94, v2
	v_mul_f32_e32 v96, v96, v3
	v_mul_f32_e32 v90, v90, v4
	v_mul_f32_e32 v92, v92, v5
	v_mul_f32_e32 v94, v94, v95
	v_mul_f32_e32 v96, v96, v97
	v_mul_f32_e32 v90, v90, v91
	v_mul_f32_e32 v92, v92, v93
	v_cvt_pk_fp8_f32 v26, v94, v96
	v_cvt_pk_fp8_f32 v26, v90, v92 op_sel:[0,0,1]
	v_min_f32_e32 v86, 0x43e00000, v86
	v_min_f32_e32 v88, 0x43e00000, v88
	v_min_f32_e32 v82, 0x43e00000, v82
	v_min_f32_e32 v84, 0x43e00000, v84
	v_mul_f32_e32 v2, 0xbd1d265f, v86
	v_mul_f32_e32 v3, 0xbd1d265f, v88
	v_mul_f32_e32 v4, 0xbd1d265f, v82
	v_mul_f32_e32 v5, 0xbd1d265f, v84
	v_exp_f32_e32 v2, v2
	v_exp_f32_e32 v3, v3
	v_exp_f32_e32 v4, v4
	v_exp_f32_e32 v5, v5
	v_fma_f32 v2, v2, v246, v246
; #define LAS __attribute__((address_space(3)))
; __device__ __forceinline__ unsigned pk4_fp8(float a, float b, float c, float d) { int w = 0; w = __builtin_amdgcn_cvt_pk_fp8_f32(a, b, w, false); w = __builtin_amdgcn_cvt_pk_fp8_f32(c, d, w, true); return (unsigned)w; }
; __device__ __forceinline__ float swiglu1(float g, float l) {
;     g = fminf(g, 7.0f); l = fminf(fmaxf(l, -7.0f), 7.0f);
;     const float s = __builtin_amdgcn_rcpf(1.0f + __expf(-1.702f * g));
;     return g * s * (l + 1.0f);
; }
;     __device__ __forceinline__ void operator()(const f32x4 (&acc)[2][2][4][2], const Unit& u, int wr, int wc, int fr, int fq) const {
;     ...
;                 for (int bj = 0; bj < 2; ++bj) { const f32x4 v0 = acc[ai][bj][m][0] * scale + bv[bj][0], v1 = acc[ai][bj][m][1] * scale + bv[bj][1];
;                     *(LAS unsigned*)(wp + m * (32 * STG8_PITCH) + 64 * bj) = pk4_fp8(swiglu1(v0[0], v0[1]), swiglu1(v0[2], v0[3]), swiglu1(v1[0], v1[1]), swiglu1(v1[2], v1[3])); }
	v_fma_f32 v3, v3, v246, v246
	v_fma_f32 v4, v4, v246, v246
	v_fma_f32 v5, v5, v246, v246
	v_rcp_f32_e32 v2, v2
	v_rcp_f32_e32 v3, v3
	v_rcp_f32_e32 v4, v4
	v_rcp_f32_e32 v5, v5
	v_med3_f32 v87, v87, s47, v204
	v_med3_f32 v89, v89, s47, v204
	v_med3_f32 v83, v83, s47, v204
	v_med3_f32 v85, v85, s47, v204
	v_mul_f32_e32 v86, v86, v2
	v_mul_f32_e32 v88, v88, v3
	v_mul_f32_e32 v82, v82, v4
	v_mul_f32_e32 v84, v84, v5
	v_mul_f32_e32 v86, v86, v87
	v_mul_f32_e32 v88, v88, v89
	v_mul_f32_e32 v82, v82, v83
	v_mul_f32_e32 v84, v84, v85
	v_cvt_pk_fp8_f32 v27, v86, v88
	v_cvt_pk_fp8_f32 v27, v82, v84 op_sel:[0,0,1]
	v_min_f32_e32 v78, 0x43e00000, v78
	v_min_f32_e32 v80, 0x43e00000, v80
	v_min_f32_e32 v74, 0x43e00000, v74
	v_min_f32_e32 v76, 0x43e00000, v76
	v_mul_f32_e32 v2, 0xbd1d265f, v78
	v_mul_f32_e32 v3, 0xbd1d265f, v80
	v_mul_f32_e32 v4, 0xbd1d265f, v74
	v_mul_f32_e32 v5, 0xbd1d265f, v76
	v_exp_f32_e32 v2, v2
	v_exp_f32_e32 v3, v3
	v_exp_f32_e32 v4, v4
	v_exp_f32_e32 v5, v5
	v_fma_f32 v2, v2, v246, v246
	v_fma_f32 v3, v3, v246, v246
	v_fma_f32 v4, v4, v246, v246
	v_fma_f32 v5, v5, v246, v246
	v_rcp_f32_e32 v2, v2
	v_rcp_f32_e32 v3, v3
	v_rcp_f32_e32 v4, v4
	v_rcp_f32_e32 v5, v5
	v_med3_f32 v79, v79, s47, v204
	v_med3_f32 v81, v81, s47, v204
	v_med3_f32 v75, v75, s47, v204
	v_med3_f32 v77, v77, s47, v204
	v_mul_f32_e32 v78, v78, v2
	v_mul_f32_e32 v80, v80, v3
	v_mul_f32_e32 v74, v74, v4
	v_mul_f32_e32 v76, v76, v5
	v_mul_f32_e32 v78, v78, v79
	v_mul_f32_e32 v80, v80, v81
	v_mul_f32_e32 v74, v74, v75
	v_mul_f32_e32 v76, v76, v77
	v_cvt_pk_fp8_f32 v28, v78, v80
	v_cvt_pk_fp8_f32 v28, v74, v76 op_sel:[0,0,1]
	v_min_f32_e32 v70, 0x43e00000, v70
	v_min_f32_e32 v72, 0x43e00000, v72
	v_min_f32_e32 v66, 0x43e00000, v66
	v_min_f32_e32 v68, 0x43e00000, v68
	v_mul_f32_e32 v2, 0xbd1d265f, v70
	v_mul_f32_e32 v3, 0xbd1d265f, v72
	v_mul_f32_e32 v4, 0xbd1d265f, v66
	v_mul_f32_e32 v5, 0xbd1d265f, v68
	v_exp_f32_e32 v2, v2
	v_exp_f32_e32 v3, v3
	v_exp_f32_e32 v4, v4
	v_exp_f32_e32 v5, v5
	v_fma_f32 v2, v2, v246, v246
	v_fma_f32 v3, v3, v246, v246
	v_fma_f32 v4, v4, v246, v246
	v_fma_f32 v5, v5, v246, v246
	v_rcp_f32_e32 v2, v2
	v_rcp_f32_e32 v3, v3
	v_rcp_f32_e32 v4, v4
	v_rcp_f32_e32 v5, v5
	v_med3_f32 v71, v71, s47, v204
	v_med3_f32 v73, v73, s47, v204
	v_med3_f32 v67, v67, s47, v204
	v_med3_f32 v69, v69, s47, v204
	v_mul_f32_e32 v70, v70, v2
	v_mul_f32_e32 v72, v72, v3
	v_mul_f32_e32 v66, v66, v4
	v_mul_f32_e32 v68, v68, v5
	v_mul_f32_e32 v70, v70, v71
	v_mul_f32_e32 v72, v72, v73
	v_mul_f32_e32 v66, v66, v67
	v_mul_f32_e32 v68, v68, v69
	v_cvt_pk_fp8_f32 v29, v70, v72
	v_cvt_pk_fp8_f32 v29, v66, v68 op_sel:[0,0,1]
	v_min_f32_e32 v58, 0x43e00000, v58
	v_min_f32_e32 v60, 0x43e00000, v60
	v_min_f32_e32 v50, 0x43e00000, v50
	v_min_f32_e32 v52, 0x43e00000, v52
	v_mul_f32_e32 v2, 0xbd1d265f, v58
	v_mul_f32_e32 v3, 0xbd1d265f, v60
	v_mul_f32_e32 v4, 0xbd1d265f, v50
	v_mul_f32_e32 v5, 0xbd1d265f, v52
	v_exp_f32_e32 v2, v2
	v_exp_f32_e32 v3, v3
	v_exp_f32_e32 v4, v4
	v_exp_f32_e32 v5, v5
	v_fma_f32 v2, v2, v246, v246
	v_fma_f32 v3, v3, v246, v246
	v_fma_f32 v4, v4, v246, v246
	v_fma_f32 v5, v5, v246, v246
	v_rcp_f32_e32 v2, v2
	v_rcp_f32_e32 v3, v3
	v_rcp_f32_e32 v4, v4
	v_rcp_f32_e32 v5, v5
	v_med3_f32 v59, v59, s47, v204
	v_med3_f32 v61, v61, s47, v204
	v_med3_f32 v51, v51, s47, v204
	v_med3_f32 v53, v53, s47, v204
	v_mul_f32_e32 v58, v58, v2
	v_mul_f32_e32 v60, v60, v3
	v_mul_f32_e32 v50, v50, v4
	v_mul_f32_e32 v52, v52, v5
	v_mul_f32_e32 v58, v58, v59
	v_mul_f32_e32 v60, v60, v61
	v_mul_f32_e32 v50, v50, v51
	v_mul_f32_e32 v52, v52, v53
	v_cvt_pk_fp8_f32 v30, v58, v60
	v_cvt_pk_fp8_f32 v30, v50, v52 op_sel:[0,0,1]
	v_min_f32_e32 v62, 0x43e00000, v62
	v_min_f32_e32 v64, 0x43e00000, v64
	v_min_f32_e32 v54, 0x43e00000, v54
	v_min_f32_e32 v56, 0x43e00000, v56
	v_mul_f32_e32 v2, 0xbd1d265f, v62
	v_mul_f32_e32 v3, 0xbd1d265f, v64
	v_mul_f32_e32 v4, 0xbd1d265f, v54
	v_mul_f32_e32 v5, 0xbd1d265f, v56
	v_exp_f32_e32 v2, v2
	v_exp_f32_e32 v3, v3
	v_exp_f32_e32 v4, v4
	v_exp_f32_e32 v5, v5
	v_fma_f32 v2, v2, v246, v246
	v_fma_f32 v3, v3, v246, v246
	v_fma_f32 v4, v4, v246, v246
	v_fma_f32 v5, v5, v246, v246
	v_rcp_f32_e32 v2, v2
	v_rcp_f32_e32 v3, v3
	v_rcp_f32_e32 v4, v4
	v_rcp_f32_e32 v5, v5
	v_med3_f32 v63, v63, s47, v204
	v_med3_f32 v65, v65, s47, v204
	v_med3_f32 v55, v55, s47, v204
; #define LAS __attribute__((address_space(3)))
; __device__ __forceinline__ unsigned pk4_fp8(float a, float b, float c, float d) { int w = 0; w = __builtin_amdgcn_cvt_pk_fp8_f32(a, b, w, false); w = __builtin_amdgcn_cvt_pk_fp8_f32(c, d, w, true); return (unsigned)w; }
;     __device__ __forceinline__ void operator()(const f32x4 (&acc)[2][2][4][2], const Unit& u, int wr, int wc, int fr, int fq) const {
;     ...
; #pragma unroll
;             for (int m = 0; m < 4; ++m)
; #pragma unroll
;                 for (int bj = 0; bj < 2; ++bj) { const f32x4 v0 = acc[ai][bj][m][0] * scale + bv[bj][0], v1 = acc[ai][bj][m][1] * scale + bv[bj][1];
;                     *(LAS unsigned*)(wp + m * (32 * STG8_PITCH) + 64 * bj) = pk4_fp8(swiglu1(v0[0], v0[1]), swiglu1(v0[2], v0[3]), swiglu1(v1[0], v1[1]), swiglu1(v1[2], v1[3])); }
;             asm volatile("s_waitcnt lgkmcnt(0)" ::: "memory"); __builtin_amdgcn_s_barrier(); asm volatile("" ::: "memory");
; #pragma unroll
;             for (int k2 = 0; k2 < 2; ++k2) { const int m = ms + 2 * k2;
;                 *(u32x4*)(gp + (size_t)(ai * HALF + m * 16) * ldc) = *(const LAS u32x4*)(rp + m * (32 * STG8_PITCH)); }
;             asm volatile("s_waitcnt lgkmcnt(0)" ::: "memory"); __builtin_amdgcn_s_barrier(); asm volatile("" ::: "memory");
;         }
	v_med3_f32 v57, v57, s47, v204
	v_mul_f32_e32 v62, v62, v2
	v_mul_f32_e32 v64, v64, v3
	v_mul_f32_e32 v54, v54, v4
	v_mul_f32_e32 v56, v56, v5
	v_mul_f32_e32 v62, v62, v63
	v_mul_f32_e32 v64, v64, v65
	v_mul_f32_e32 v54, v54, v55
	v_mul_f32_e32 v56, v56, v57
	v_cvt_pk_fp8_f32 v31, v62, v64
	v_cvt_pk_fp8_f32 v31, v54, v56 op_sel:[0,0,1]
	v_min_f32_e32 v38, 0x43e00000, v38
	v_min_f32_e32 v40, 0x43e00000, v40
	v_min_f32_e32 v34, 0x43e00000, v34
	v_min_f32_e32 v36, 0x43e00000, v36
	v_mul_f32_e32 v2, 0xbd1d265f, v38
	v_mul_f32_e32 v3, 0xbd1d265f, v40
	v_mul_f32_e32 v4, 0xbd1d265f, v34
	v_mul_f32_e32 v5, 0xbd1d265f, v36
	v_exp_f32_e32 v2, v2
	v_exp_f32_e32 v3, v3
	v_exp_f32_e32 v4, v4
	v_exp_f32_e32 v5, v5
	v_fma_f32 v2, v2, v246, v246
	v_fma_f32 v3, v3, v246, v246
	v_fma_f32 v4, v4, v246, v246
	v_fma_f32 v5, v5, v246, v246
	v_rcp_f32_e32 v2, v2
	v_rcp_f32_e32 v3, v3
	v_rcp_f32_e32 v4, v4
	v_rcp_f32_e32 v5, v5
	v_med3_f32 v39, v39, s47, v204
	v_med3_f32 v41, v41, s47, v204
	v_med3_f32 v35, v35, s47, v204
	v_med3_f32 v37, v37, s47, v204
	v_mul_f32_e32 v38, v38, v2
	v_mul_f32_e32 v40, v40, v3
	v_mul_f32_e32 v34, v34, v4
	v_mul_f32_e32 v36, v36, v5
	v_mul_f32_e32 v38, v38, v39
	v_mul_f32_e32 v40, v40, v41
	v_mul_f32_e32 v34, v34, v35
	v_mul_f32_e32 v36, v36, v37
	v_cvt_pk_fp8_f32 v32, v38, v40
	v_cvt_pk_fp8_f32 v32, v34, v36 op_sel:[0,0,1]
	v_min_f32_e32 v46, 0x43e00000, v46
	v_min_f32_e32 v48, 0x43e00000, v48
	v_min_f32_e32 v42, 0x43e00000, v42
	v_min_f32_e32 v44, 0x43e00000, v44
	v_mul_f32_e32 v2, 0xbd1d265f, v46
	v_mul_f32_e32 v3, 0xbd1d265f, v48
	v_mul_f32_e32 v4, 0xbd1d265f, v42
	v_mul_f32_e32 v5, 0xbd1d265f, v44
	v_exp_f32_e32 v2, v2
	v_exp_f32_e32 v3, v3
	v_exp_f32_e32 v4, v4
	v_exp_f32_e32 v5, v5
	v_fma_f32 v2, v2, v246, v246
	v_fma_f32 v3, v3, v246, v246
	v_fma_f32 v4, v4, v246, v246
	v_fma_f32 v5, v5, v246, v246
	v_rcp_f32_e32 v2, v2
	v_rcp_f32_e32 v3, v3
	v_rcp_f32_e32 v4, v4
	v_rcp_f32_e32 v5, v5
	v_med3_f32 v47, v47, s47, v204
	v_med3_f32 v49, v49, s47, v204
	v_med3_f32 v43, v43, s47, v204
	v_med3_f32 v45, v45, s47, v204
	v_mul_f32_e32 v46, v46, v2
	v_mul_f32_e32 v48, v48, v3
	v_mul_f32_e32 v42, v42, v4
	v_mul_f32_e32 v44, v44, v5
	v_mul_f32_e32 v46, v46, v47
	v_mul_f32_e32 v48, v48, v49
	v_mul_f32_e32 v42, v42, v43
	v_mul_f32_e32 v44, v44, v45
	v_cvt_pk_fp8_f32 v33, v46, v48
	v_cvt_pk_fp8_f32 v33, v42, v44 op_sel:[0,0,1]
	v_add_u32_e32 v14, 0xfffe7000, v202
	v_add_u32_e32 v15, 0xfffe8000, v202
	v_add_u32_e32 v16, 0xfffe9400, v202
	v_add_u32_e32 v17, 0xfffea400, v202
	ds_write2_b32 v202, v6, v7 offset1:16
	ds_write2_b32 v22, v8, v9 offset0:128 offset1:144
	ds_write2_b32 v23, v10, v11 offset1:16
	ds_write2_b32 v24, v12, v13 offset0:128 offset1:144
	ds_write2_b32 v14, v26, v27 offset1:16
	ds_write2_b32 v15, v28, v29 offset0:128 offset1:144
	ds_write2_b32 v16, v30, v31 offset1:16
	ds_write2_b32 v17, v32, v33 offset0:128 offset1:144
	s_waitcnt lgkmcnt(0)
	s_barrier
	v_add_u32_e32 v14, 0xfffe7000, v203
	ds_read_b128 v[26:29], v203
	ds_read_b128 v[30:33], v203 offset:9216
	ds_read_b128 v[2:5], v14
	ds_read_b128 v[6:9], v14 offset:9216
	v_lshl_add_u64 v[20:21], v[18:19], 0, v[172:173]
	v_lshl_add_u64 v[18:19], v[18:19], 0, v[174:175]
	v_add_co_u32_e32 v10, vcc, s48, v20
	s_nop 1
	v_addc_co_u32_e32 v11, vcc, 0, v21, vcc
	v_add_co_u32_e32 v12, vcc, 0x40000, v18
	s_nop 1
	v_addc_co_u32_e32 v13, vcc, 0, v19, vcc
	s_waitcnt lgkmcnt(3)
	global_store_dwordx4 v[20:21], v[26:29], off
	s_waitcnt lgkmcnt(2)
	global_store_dwordx4 v[18:19], v[30:33], off
	s_waitcnt lgkmcnt(1)
	global_store_dwordx4 v[10:11], v[2:5], off
	s_waitcnt lgkmcnt(0)
	global_store_dwordx4 v[12:13], v[6:9], off
	s_barrier
	s_waitcnt vmcnt(4)
	v_mul_f32_e32 v208, v247, v208
	v_fma_f32 v209, v209, v247, v247
	v_mul_f32_e32 v210, v247, v210
	v_fma_f32 v211, v211, v247, v247
	v_mul_f32_e32 v212, v247, v212
	v_fma_f32 v213, v213, v247, v247
	v_mul_f32_e32 v214, v247, v214
	v_fma_f32 v215, v215, v247, v247
	v_mul_f32_e32 v216, v247, v216
	v_fma_f32 v217, v217, v247, v247
	v_mul_f32_e32 v218, v247, v218
	v_fma_f32 v219, v219, v247, v247
	v_mul_f32_e32 v220, v247, v220
	v_fma_f32 v221, v221, v247, v247
	v_mul_f32_e32 v222, v247, v222
	v_fma_f32 v223, v223, v247, v247
	s_cbranch_scc1 .LBB0_993
	s_andn2_b64 vcc, exec, s[6:7]
	s_cbranch_vccnz .LBB0_992
	s_barrier
	s_branch .LBB0_992

; #define LAS __attribute__((address_space(3)))
; __device__ __forceinline__ unsigned pk4_fp8(float a, float b, float c, float d) { int w = 0; w = __builtin_amdgcn_cvt_pk_fp8_f32(a, b, w, false); w = __builtin_amdgcn_cvt_pk_fp8_f32(c, d, w, true); return (unsigned)w; }
;     __device__ __forceinline__ void operator()(const f32x4 (&acc)[2][2][4][2], const Unit& u, int wr, int wc, int fr, int fq) const {
;         const int e = u.pn / npn, pnl = u.pn - e * npn; const int tid = threadIdx.x;
;         const int col0 = pnl * BM + wc * 32 + 8 * fq;
;         f32x4 bv[2][2];
; #pragma unroll
;         for (int bj = 0; bj < 2; ++bj)
; #pragma unroll
;             for (int n = 0; n < 2; ++n) bv[bj][n] = *(const f32x4*)(bias + (size_t)e * bias_ld + col0 + bj * HALF + 4 * n);
;         constexpr int PITCH = 272, SLAB = 32 * PITCH;
;         LAS unsigned char* wp = stg + (16 * wr + fr) * PITCH + 32 * wc + 8 * fq;
;         const int rr = tid >> 4, cc = tid & 15; const LAS unsigned char* rp = stg + rr * PITCH + cc * 16;
;         unsigned char* gp = O + (size_t)(u.pm * BM + 64 * (rr >> 4) + (rr & 15)) * ldc + pnl * BM + cc * 16;
; #pragma unroll
;         for (int ai = 0; ai < 2; ++ai)
; #pragma unroll
;             for (int mp = 0; mp < 2; ++mp) {
; #pragma unroll
;                 for (int ms = 0; ms < 2; ++ms)
; #pragma unroll
;                     for (int bj = 0; bj < 2; ++bj) { const int m = 2 * mp + ms; const f32x4 v0 = acc[ai][bj][m][0] * scale + bv[bj][0], v1 = acc[ai][bj][m][1] * scale + bv[bj][1];
;                         u32x2 w; w.x = pk4_fp8(v0[0], v0[1], v0[2], v0[3]); w.y = pk4_fp8(v1[0], v1[1], v1[2], v1[3]);
;                         *(LAS u32x2*)(wp + ms * SLAB + 128 * bj) = w; }
.LBB0_1150:
	s_ashr_i32 s2, s21, 31
	s_lshr_b32 s2, s2, 29
	s_add_i32 s2, s21, s2
	s_ashr_i32 s2, s2, 3
	s_lshl_b32 s3, s2, 11
	s_lshl_b32 s21, s21, 8
	v_readlane_b32 s56, v254, 0
	s_sub_i32 s22, s21, s3
	s_ashr_i32 s3, s2, 31
	v_readlane_b32 s60, v254, 4
	v_readlane_b32 s61, v254, 5
	s_lshl_b64 s[2:3], s[2:3], 13
	v_readlane_b32 s62, v254, 6
	v_readlane_b32 s63, v254, 7
	s_mov_b64 s[24:25], s[60:61]
	v_or_b32_e32 v2, s22, v186
	s_add_u32 s2, s24, s2
	s_addc_u32 s3, s25, s3
	v_ashrrev_i32_e32 v3, 31, v2
	s_nop 11
	v_lshl_add_u64 v[2:3], v[2:3], 2, s[2:3]
	global_load_dwordx4 v[14:17], v[2:3], off
	global_load_dwordx4 v[10:13], v[2:3], off offset:16
	global_load_dwordx4 v[6:9], v[2:3], off offset:512
	s_nop 0
	global_load_dwordx4 v[2:5], v[2:3], off offset:528
	v_mov_b32_e32 v20, 0
	v_mov_b32_e32 v21, 0
	v_mov_b32_e32 v22, 0
	v_mov_b32_e32 v23, 0
	v_mov_b32_e32 v24, 0
	v_mov_b32_e32 v25, 0
	v_mov_b32_e32 v26, 0
	v_mov_b32_e32 v27, 0
	v_lshl_or_b32 v18, s20, 8, v187
	v_add_u32_e32 v178, 0x2000, v188
	v_ashrrev_i32_e32 v19, 31, v18
	v_lshlrev_b64 v[18:19], 11, v[18:19]
	v_mov_b32_e32 v32, 0
	v_mov_b32_e32 v33, 0
	v_lshl_add_u64 v[18:19], s[4:5], 0, v[18:19]
	s_ashr_i32 s23, s22, 31
	v_lshl_add_u64 v[18:19], v[18:19], 0, s[22:23]
	v_lshl_add_u64 v[18:19], v[18:19], 0, v[170:171]
	v_add_co_u32_e32 v176, vcc, s50, v18
	v_mov_b32_e32 v28, 0
	v_mov_b32_e32 v29, 0
	v_mov_b32_e32 v30, 0
	v_mov_b32_e32 v31, 0
	v_addc_co_u32_e32 v177, vcc, 0, v19, vcc
	s_cmp_eq_u32 s49, s48
	s_mov_b64 s[2:3], -1
	v_readlane_b32 s57, v254, 1
	v_readlane_b32 s58, v254, 2
	v_readlane_b32 s59, v254, 3
	s_mov_b64 s[26:27], s[62:63]
	s_waitcnt vmcnt(0)
	v_pk_fma_f32 v[158:159], v[158:159], s[12:13], v[14:15] op_sel_hi:[1,0,1]
	v_pk_fma_f32 v[154:155], v[154:155], s[12:13], v[10:11] op_sel_hi:[1,0,1]
	v_pk_fma_f32 v[138:139], v[138:139], s[12:13], v[6:7] op_sel_hi:[1,0,1]
	v_pk_fma_f32 v[130:131], v[130:131], s[12:13], v[2:3] op_sel_hi:[1,0,1]
	v_pk_fma_f32 v[150:151], v[150:151], s[12:13], v[14:15] op_sel_hi:[1,0,1]
	v_pk_fma_f32 v[146:147], v[146:147], s[12:13], v[10:11] op_sel_hi:[1,0,1]
	v_pk_fma_f32 v[126:127], v[126:127], s[12:13], v[6:7] op_sel_hi:[1,0,1]
	v_pk_fma_f32 v[122:123], v[122:123], s[12:13], v[2:3] op_sel_hi:[1,0,1]
	v_cvt_pk_fp8_f32 v20, v158, v159
	v_cvt_pk_fp8_f32 v21, v154, v155
	v_cvt_pk_fp8_f32 v22, v138, v139
	v_cvt_pk_fp8_f32 v23, v130, v131
	v_cvt_pk_fp8_f32 v24, v150, v151
	v_cvt_pk_fp8_f32 v25, v146, v147
	v_cvt_pk_fp8_f32 v26, v126, v127
	v_cvt_pk_fp8_f32 v27, v122, v123
	v_pk_fma_f32 v[160:161], v[160:161], s[12:13], v[16:17] op_sel_hi:[1,0,1]
	v_pk_fma_f32 v[156:157], v[156:157], s[12:13], v[12:13] op_sel_hi:[1,0,1]
	v_pk_fma_f32 v[140:141], v[140:141], s[12:13], v[8:9] op_sel_hi:[1,0,1]
	v_pk_fma_f32 v[132:133], v[132:133], s[12:13], v[4:5] op_sel_hi:[1,0,1]
	v_pk_fma_f32 v[152:153], v[152:153], s[12:13], v[16:17] op_sel_hi:[1,0,1]
	v_pk_fma_f32 v[148:149], v[148:149], s[12:13], v[12:13] op_sel_hi:[1,0,1]
	v_pk_fma_f32 v[128:129], v[128:129], s[12:13], v[8:9] op_sel_hi:[1,0,1]
	v_pk_fma_f32 v[124:125], v[124:125], s[12:13], v[4:5] op_sel_hi:[1,0,1]
	v_cvt_pk_fp8_f32 v20, v160, v161 op_sel:[0,0,1]
	v_cvt_pk_fp8_f32 v21, v156, v157 op_sel:[0,0,1]
	v_cvt_pk_fp8_f32 v22, v140, v141 op_sel:[0,0,1]
	v_cvt_pk_fp8_f32 v23, v132, v133 op_sel:[0,0,1]
	v_cvt_pk_fp8_f32 v24, v152, v153 op_sel:[0,0,1]
	v_cvt_pk_fp8_f32 v25, v148, v149 op_sel:[0,0,1]
	v_cvt_pk_fp8_f32 v26, v128, v129 op_sel:[0,0,1]
	v_cvt_pk_fp8_f32 v27, v124, v125 op_sel:[0,0,1]
	ds_write2_b64 v188, v[20:21], v[22:23] offset1:16
	ds_write2_b64 v178, v[24:25], v[26:27] offset0:64 offset1:80
	s_waitcnt lgkmcnt(0)
	s_barrier
	ds_read_b128 v[20:23], v189
	ds_read_b128 v[24:27], v189 offset:8704
	v_pk_fma_f32 v[110:111], v[110:111], s[12:13], v[14:15] op_sel_hi:[1,0,1]
	v_pk_fma_f32 v[106:107], v[106:107], s[12:13], v[10:11] op_sel_hi:[1,0,1]
	v_cvt_pk_fp8_f32 v32, v110, v111
	v_cvt_pk_fp8_f32 v33, v106, v107
	v_pk_fma_f32 v[142:143], v[142:143], s[12:13], v[14:15] op_sel_hi:[1,0,1]
	v_pk_fma_f32 v[134:135], v[134:135], s[12:13], v[10:11] op_sel_hi:[1,0,1]
	v_pk_fma_f32 v[118:119], v[118:119], s[12:13], v[6:7] op_sel_hi:[1,0,1]
	v_pk_fma_f32 v[114:115], v[114:115], s[12:13], v[2:3] op_sel_hi:[1,0,1]
	s_waitcnt lgkmcnt(1)
	global_store_dwordx4 v[18:19], v[20:23], off
	s_waitcnt lgkmcnt(0)
	global_store_dwordx4 v[176:177], v[24:27], off
	v_cvt_pk_fp8_f32 v28, v142, v143
	v_pk_fma_f32 v[20:21], v[112:113], s[12:13], v[16:17] op_sel_hi:[1,0,1]
	v_pk_fma_f32 v[22:23], v[108:109], s[12:13], v[12:13] op_sel_hi:[1,0,1]
	v_cvt_pk_fp8_f32 v29, v134, v135
	v_cvt_pk_fp8_f32 v30, v118, v119
	v_cvt_pk_fp8_f32 v31, v114, v115
	v_cvt_pk_fp8_f32 v32, v20, v21 op_sel:[0,0,1]
	v_cvt_pk_fp8_f32 v33, v22, v23 op_sel:[0,0,1]
	v_pk_fma_f32 v[20:21], v[102:103], s[12:13], v[6:7] op_sel_hi:[1,0,1]
	v_pk_fma_f32 v[22:23], v[98:99], s[12:13], v[2:3] op_sel_hi:[1,0,1]
	v_mov_b32_e32 v24, 0
	v_mov_b32_e32 v25, 0
	v_cvt_pk_fp8_f32 v24, v20, v21
	v_cvt_pk_fp8_f32 v25, v22, v23
	v_pk_fma_f32 v[144:145], v[144:145], s[12:13], v[16:17] op_sel_hi:[1,0,1]
	v_pk_fma_f32 v[136:137], v[136:137], s[12:13], v[12:13] op_sel_hi:[1,0,1]
	v_pk_fma_f32 v[120:121], v[120:121], s[12:13], v[8:9] op_sel_hi:[1,0,1]
	v_pk_fma_f32 v[116:117], v[116:117], s[12:13], v[4:5] op_sel_hi:[1,0,1]
	v_cvt_pk_fp8_f32 v28, v144, v145 op_sel:[0,0,1]
	v_cvt_pk_fp8_f32 v29, v136, v137 op_sel:[0,0,1]
	v_cvt_pk_fp8_f32 v30, v120, v121 op_sel:[0,0,1]
	v_cvt_pk_fp8_f32 v31, v116, v117 op_sel:[0,0,1]
	v_pk_fma_f32 v[20:21], v[104:105], s[12:13], v[8:9] op_sel_hi:[1,0,1]
	v_pk_fma_f32 v[22:23], v[100:101], s[12:13], v[4:5] op_sel_hi:[1,0,1]
	v_cvt_pk_fp8_f32 v24, v20, v21 op_sel:[0,0,1]
	v_cvt_pk_fp8_f32 v25, v22, v23 op_sel:[0,0,1]
	s_waitcnt lgkmcnt(0)
	s_barrier
; #define LAS __attribute__((address_space(3)))
; __device__ __forceinline__ unsigned pk4_fp8(float a, float b, float c, float d) { int w = 0; w = __builtin_amdgcn_cvt_pk_fp8_f32(a, b, w, false); w = __builtin_amdgcn_cvt_pk_fp8_f32(c, d, w, true); return (unsigned)w; }
;     __device__ __forceinline__ void operator()(const f32x4 (&acc)[2][2][4][2], const Unit& u, int wr, int wc, int fr, int fq) const {
;     ...
; #pragma unroll
;         for (int ai = 0; ai < 2; ++ai)
; #pragma unroll
;             for (int mp = 0; mp < 2; ++mp) {
; #pragma unroll
;                 for (int ms = 0; ms < 2; ++ms)
; #pragma unroll
;                     for (int bj = 0; bj < 2; ++bj) { const int m = 2 * mp + ms; const f32x4 v0 = acc[ai][bj][m][0] * scale + bv[bj][0], v1 = acc[ai][bj][m][1] * scale + bv[bj][1];
;                         u32x2 w; w.x = pk4_fp8(v0[0], v0[1], v0[2], v0[3]); w.y = pk4_fp8(v1[0], v1[1], v1[2], v1[3]);
;                         *(LAS u32x2*)(wp + ms * SLAB + 128 * bj) = w; }
;                 asm volatile("s_waitcnt lgkmcnt(0)" ::: "memory"); __builtin_amdgcn_s_barrier(); asm volatile("" ::: "memory");
; #pragma unroll
;                 for (int ms = 0; ms < 2; ++ms) *(u32x4*)(gp + (size_t)(ai * HALF + (2 * mp + ms) * 16) * ldc) = *(const LAS u32x4*)(rp + ms * SLAB);
;                 asm volatile("s_waitcnt lgkmcnt(0)" ::: "memory"); __builtin_amdgcn_s_barrier(); asm volatile("" ::: "memory");
;             }
	ds_write2_b64 v188, v[28:29], v[30:31] offset1:16
	ds_write2_b64 v178, v[32:33], v[24:25] offset0:64 offset1:80
	s_waitcnt lgkmcnt(0)
	s_barrier
	ds_read_b128 v[20:23], v189
	ds_read_b128 v[24:27], v189 offset:8704
	v_add_co_u32_e32 v28, vcc, s51, v18
	v_mov_b32_e32 v30, 0
	s_nop 0
	v_addc_co_u32_e32 v29, vcc, 0, v19, vcc
	s_waitcnt lgkmcnt(1)
	global_store_dwordx4 v[28:29], v[20:23], off
	v_mov_b32_e32 v28, 0
	v_mov_b32_e32 v29, 0
	v_add_co_u32_e32 v20, vcc, s47, v18
	v_pk_fma_f32 v[22:23], v[90:91], s[12:13], v[10:11] op_sel_hi:[1,0,1]
	s_nop 0
	v_addc_co_u32_e32 v21, vcc, 0, v19, vcc
	s_waitcnt lgkmcnt(0)
	global_store_dwordx4 v[20:21], v[24:27], off
	v_pk_fma_f32 v[20:21], v[94:95], s[12:13], v[14:15] op_sel_hi:[1,0,1]
	v_mov_b32_e32 v31, 0
	v_mov_b32_e32 v24, 0
	v_mov_b32_e32 v25, 0
	v_cvt_pk_fp8_f32 v24, v20, v21
	v_cvt_pk_fp8_f32 v25, v22, v23
	v_pk_fma_f32 v[20:21], v[96:97], s[12:13], v[16:17] op_sel_hi:[1,0,1]
	v_pk_fma_f32 v[22:23], v[92:93], s[12:13], v[12:13] op_sel_hi:[1,0,1]
	v_cvt_pk_fp8_f32 v24, v20, v21 op_sel:[0,0,1]
	v_cvt_pk_fp8_f32 v25, v22, v23 op_sel:[0,0,1]
	v_pk_fma_f32 v[20:21], v[82:83], s[12:13], v[6:7] op_sel_hi:[1,0,1]
	v_pk_fma_f32 v[22:23], v[74:75], s[12:13], v[2:3] op_sel_hi:[1,0,1]
	v_mov_b32_e32 v26, 0
	v_mov_b32_e32 v27, 0
	v_cvt_pk_fp8_f32 v26, v20, v21
	v_cvt_pk_fp8_f32 v27, v22, v23
	v_pk_fma_f32 v[20:21], v[84:85], s[12:13], v[8:9] op_sel_hi:[1,0,1]
	v_pk_fma_f32 v[22:23], v[76:77], s[12:13], v[4:5] op_sel_hi:[1,0,1]
	v_cvt_pk_fp8_f32 v26, v20, v21 op_sel:[0,0,1]
	v_cvt_pk_fp8_f32 v27, v22, v23 op_sel:[0,0,1]
	v_pk_fma_f32 v[20:21], v[86:87], s[12:13], v[14:15] op_sel_hi:[1,0,1]
	v_pk_fma_f32 v[22:23], v[78:79], s[12:13], v[10:11] op_sel_hi:[1,0,1]
	v_cvt_pk_fp8_f32 v28, v20, v21
	v_cvt_pk_fp8_f32 v29, v22, v23
	v_pk_fma_f32 v[20:21], v[88:89], s[12:13], v[16:17] op_sel_hi:[1,0,1]
	v_pk_fma_f32 v[22:23], v[80:81], s[12:13], v[12:13] op_sel_hi:[1,0,1]
	v_cvt_pk_fp8_f32 v28, v20, v21 op_sel:[0,0,1]
	v_cvt_pk_fp8_f32 v29, v22, v23 op_sel:[0,0,1]
	v_pk_fma_f32 v[20:21], v[70:71], s[12:13], v[6:7] op_sel_hi:[1,0,1]
	v_pk_fma_f32 v[22:23], v[66:67], s[12:13], v[2:3] op_sel_hi:[1,0,1]
	v_cvt_pk_fp8_f32 v30, v20, v21
	v_cvt_pk_fp8_f32 v31, v22, v23
	v_pk_fma_f32 v[20:21], v[72:73], s[12:13], v[8:9] op_sel_hi:[1,0,1]
	v_pk_fma_f32 v[22:23], v[68:69], s[12:13], v[4:5] op_sel_hi:[1,0,1]
	v_cvt_pk_fp8_f32 v30, v20, v21 op_sel:[0,0,1]
	v_cvt_pk_fp8_f32 v31, v22, v23 op_sel:[0,0,1]
	s_waitcnt lgkmcnt(0)
	s_barrier
	ds_write2_b64 v188, v[24:25], v[26:27] offset1:16
	ds_write2_b64 v178, v[28:29], v[30:31] offset0:64 offset1:80
	s_waitcnt lgkmcnt(0)
	s_barrier
	ds_read_b128 v[20:23], v189
	ds_read_b128 v[24:27], v189 offset:8704
	v_add_co_u32_e32 v28, vcc, s52, v18
	s_nop 1
	v_addc_co_u32_e32 v29, vcc, 0, v19, vcc
	s_waitcnt lgkmcnt(1)
	global_store_dwordx4 v[28:29], v[20:23], off
	s_nop 1
	v_add_co_u32_e32 v20, vcc, s53, v18
	v_pk_fma_f32 v[22:23], v[58:59], s[12:13], v[10:11] op_sel_hi:[1,0,1]
	s_nop 0
	v_addc_co_u32_e32 v21, vcc, 0, v19, vcc
	s_waitcnt lgkmcnt(0)
	global_store_dwordx4 v[20:21], v[24:27], off
	v_pk_fma_f32 v[20:21], v[62:63], s[12:13], v[14:15] op_sel_hi:[1,0,1]
	v_pk_fma_f32 v[14:15], v[54:55], s[12:13], v[14:15] op_sel_hi:[1,0,1]
	v_mov_b32_e32 v24, 0
	v_cvt_pk_fp8_f32 v24, v20, v21
	v_pk_fma_f32 v[20:21], v[64:65], s[12:13], v[16:17] op_sel_hi:[1,0,1]
	v_mov_b32_e32 v26, 0
	v_mov_b32_e32 v25, 0
	v_cvt_pk_fp8_f32 v24, v20, v21 op_sel:[0,0,1]
	v_pk_fma_f32 v[20:21], v[50:51], s[12:13], v[6:7] op_sel_hi:[1,0,1]
	v_cvt_pk_fp8_f32 v25, v22, v23
	v_cvt_pk_fp8_f32 v26, v20, v21
	v_pk_fma_f32 v[20:21], v[52:53], s[12:13], v[8:9] op_sel_hi:[1,0,1]
	v_pk_fma_f32 v[22:23], v[60:61], s[12:13], v[12:13] op_sel_hi:[1,0,1]
	v_pk_fma_f32 v[10:11], v[46:47], s[12:13], v[10:11] op_sel_hi:[1,0,1]
	v_cvt_pk_fp8_f32 v26, v20, v21 op_sel:[0,0,1]
	v_mov_b32_e32 v20, 0
	v_cvt_pk_fp8_f32 v20, v14, v15
	v_mov_b32_e32 v21, 0
	v_cvt_pk_fp8_f32 v25, v22, v23 op_sel:[0,0,1]
	v_pk_fma_f32 v[22:23], v[42:43], s[12:13], v[2:3] op_sel_hi:[1,0,1]
	v_mov_b32_e32 v27, 0
	v_cvt_pk_fp8_f32 v21, v10, v11
	v_pk_fma_f32 v[10:11], v[56:57], s[12:13], v[16:17] op_sel_hi:[1,0,1]
	v_cvt_pk_fp8_f32 v27, v22, v23
	v_cvt_pk_fp8_f32 v20, v10, v11 op_sel:[0,0,1]
	v_pk_fma_f32 v[6:7], v[38:39], s[12:13], v[6:7] op_sel_hi:[1,0,1]
	v_pk_fma_f32 v[2:3], v[34:35], s[12:13], v[2:3] op_sel_hi:[1,0,1]
	v_mov_b32_e32 v10, 0
	v_mov_b32_e32 v11, 0
	v_cvt_pk_fp8_f32 v10, v6, v7
	v_cvt_pk_fp8_f32 v11, v2, v3
	v_pk_fma_f32 v[22:23], v[44:45], s[12:13], v[4:5] op_sel_hi:[1,0,1]
	v_pk_fma_f32 v[12:13], v[48:49], s[12:13], v[12:13] op_sel_hi:[1,0,1]
	v_cvt_pk_fp8_f32 v27, v22, v23 op_sel:[0,0,1]
	v_pk_fma_f32 v[2:3], v[40:41], s[12:13], v[8:9] op_sel_hi:[1,0,1]
	v_pk_fma_f32 v[4:5], v[36:37], s[12:13], v[4:5] op_sel_hi:[1,0,1]
	v_cvt_pk_fp8_f32 v21, v12, v13 op_sel:[0,0,1]
	v_cvt_pk_fp8_f32 v10, v2, v3 op_sel:[0,0,1]
	v_cvt_pk_fp8_f32 v11, v4, v5 op_sel:[0,0,1]
	s_waitcnt lgkmcnt(0)
	s_barrier
	ds_write2_b64 v188, v[24:25], v[26:27] offset1:16
	ds_write2_b64 v178, v[20:21], v[10:11] offset0:64 offset1:80
	s_waitcnt lgkmcnt(0)
	s_barrier
	ds_read_b128 v[2:5], v189
	ds_read_b128 v[6:9], v189 offset:8704
	v_add_co_u32_e32 v10, vcc, 0x50000, v18
	s_nop 1
	v_addc_co_u32_e32 v11, vcc, 0, v19, vcc
	s_waitcnt lgkmcnt(1)
	global_store_dwordx4 v[10:11], v[2:5], off
	s_nop 1
	v_add_co_u32_e32 v2, vcc, 0x58000, v18
	s_nop 1
	v_addc_co_u32_e32 v3, vcc, 0, v19, vcc
	s_waitcnt lgkmcnt(0)
	global_store_dwordx4 v[2:3], v[6:9], off
	s_waitcnt lgkmcnt(0)
	s_barrier
	s_cbranch_scc1 .LBB0_1143
	s_andn2_b64 vcc, exec, s[0:1]
	s_cbranch_vccnz .LBB0_1142
	s_barrier
	s_branch .LBB0_1142
